# hgrn in-projection: column tile rotated by 4 per round so every workgroup gets a mix of silu/sigmoid/plain epilogues; swa sink load issued ahead of the K/V staging wait
# speedup vs baseline: 1.0217x; 1.0017x over previous
.LBB0_596:
	s_add_i32 s47, s16, 1
	v_readlane_b32 s12, v246, 43
	s_mul_i32 s12, s47, s12
	v_readlane_b32 s13, v243, 52
	s_add_i32 s12, s12, s13
	s_ashr_i32 s13, s12, 31
	s_lshr_b32 s13, s13, 28
	s_add_i32 s13, s12, s13
	s_ashr_i32 s14, s13, 4
	s_and_b32 s13, s13, -16
	s_sub_i32 s12, s12, s13
	s_lshl_b32 s13, s47, 2
	s_add_i32 s12, s12, s13
	s_and_b32 s12, s12, 15
	s_lshl_b32 s13, s14, 3
	v_readlane_b32 s14, v243, 0
	s_or_b32 s50, s13, s14
	s_cmpk_lt_i32 s50, 0x80
	s_cselect_b64 s[14:15], -1, 0
	s_cmpk_gt_i32 s50, 0x7f
	s_cbranch_scc1 .LBB0_598
	s_lshl_b32 s10, s50, 8
	v_add_u32_e32 v2, s10, v1
	v_lshl_add_u32 v218, v2, 10, v194
	v_add_u32_e32 v2, s10, v211
	s_bitset1_b32 s10, 7
	v_lshl_add_u32 v219, v2, 10, v212
	v_add_u32_e32 v2, s10, v1
	s_ashr_i32 s13, s12, 31
	v_lshl_add_u32 v220, v2, 10, v194
	v_add_u32_e32 v2, s10, v211
	s_lshl_b64 s[10:11], s[12:13], 18
	v_readlane_b32 s13, v245, 54
	s_add_u32 s10, s13, s10
	v_readlane_b32 s13, v245, 55
	v_lshl_add_u32 v221, v2, 10, v212
	s_addc_u32 s11, s13, s11

.LBB0_1880:
	v_readlane_b32 s50, v242, 10
	s_add_i32 s58, s62, s50
	s_lshr_b32 s51, s58, 3
	s_and_b32 s51, s51, 12
	s_add_i32 s54, s51, s60
	s_ashr_i32 s55, s54, 31
	s_and_b32 s56, s58, 31
	s_ashr_i32 s50, s58, 7
	s_lshl_b64 s[52:53], s[54:55], 2
	v_readlane_b32 s68, v244, 27
	v_readlane_b32 s69, v244, 28
	s_add_u32 s52, s68, s52
	s_addc_u32 s53, s69, s53
	global_load_dword v181, v195, s[52:53]
	s_waitcnt vmcnt(1)
	ds_write_b128 v173, v[118:121]
	ds_write_b128 v174, v[126:129] offset:36864
	ds_write_b128 v175, v[106:109]
	ds_write_b128 v176, v[122:125] offset:36864
	ds_write_b128 v177, v[102:105]
	ds_write_b128 v178, v[114:117] offset:36864
	ds_write_b128 v179, v[98:101]
	ds_write_b128 v180, v[110:113] offset:36864
	s_waitcnt lgkmcnt(0)
	s_barrier
	v_readlane_b32 s52, v242, 16
	v_readlane_b32 s53, v242, 17
	s_ashr_i32 s51, s50, 31
	s_lshl_b64 s[50:51], s[50:51], 12
	v_mov_b64_e32 v[2:3], s[52:53]
	s_lshl_b32 s52, s56, 7
	s_or_b32 s50, s50, s52
	s_cmp_eq_u32 s56, 0
	v_or_b32_e32 v4, s50, v144
	s_movk_i32 s67, 0xc00
	s_cselect_b64 s[52:53], -1, 0
	s_lshl_b32 s54, s54, 6
	v_mad_u64_u32 v[4:5], s[56:57], v4, s67, v[2:3]
	s_ashr_i32 s55, s54, 31
	v_readlane_b32 s56, v242, 4
	v_mad_i32_i24 v5, s51, v207, v5
	s_cmp_lt_i32 s62, s56
	v_lshl_add_u64 v[148:149], v[142:143], 0, s[54:55]
	v_lshl_add_u64 v[4:5], s[54:55], 1, v[4:5]
	s_cselect_b64 s[54:55], -1, 0
	s_add_i32 s58, s58, 1
	s_and_b32 s57, s58, 31
	s_bfe_u32 s59, s58, 0x20005
	s_ashr_i32 s56, s58, 7
	s_lshl_b32 s58, s57, 7
	s_add_i32 s63, s58, 0xffffff80
	s_cmp_lg_u32 s57, 0
	v_mov_b32_e32 v16, s63
	s_cselect_b32 s63, s63, 0
	s_ashr_i32 s57, s56, 31
	v_lshl_add_u64 v[150:151], v[4:5], 0, v[194:195]
	v_or_b32_e32 v4, s58, v165
	v_readlane_b32 s68, v244, 23
	s_lshl_b64 s[56:57], s[56:57], 12
	v_mov_b32_e32 v17, s63
	s_lshl_b32 s58, s59, 8
	v_readlane_b32 s69, v244, 24
	v_or_b32_e32 v4, s56, v4
	v_cndmask_b32_e64 v6, v16, v17, s[6:7]
	s_mov_b32 s71, s69
	s_add_i32 s58, s58, s61
	v_cndmask_b32_e64 v7, v16, v17, s[4:5]
	v_cndmask_b32_e64 v9, v16, v17, s[44:45]
	v_mad_u64_u32 v[4:5], s[68:69], v4, s67, v[2:3]
	v_add_u32_e32 v6, v6, v1
	s_lshl_b32 s70, s59, 7
	s_ashr_i32 s59, s58, 31
	v_add_u32_e32 v8, v7, v145
	v_add_u32_e32 v10, v9, v162
	v_mad_i32_i24 v5, s57, v207, v5
	v_ashrrev_i32_e32 v7, 31, v6
	v_ashrrev_i32_e32 v11, 31, v10
	v_lshl_add_u64 v[4:5], s[58:59], 1, v[4:5]
	v_lshl_add_u64 v[6:7], s[56:57], 0, v[6:7]
	v_lshl_add_u64 v[10:11], s[56:57], 0, v[10:11]
	v_lshl_add_u64 v[152:153], v[4:5], 0, v[194:195]
	v_mad_u64_u32 v[4:5], s[58:59], v6, s67, v[2:3]
	v_mad_u64_u32 v[14:15], s[58:59], v10, s67, v[2:3]
	v_mad_i32_i24 v5, v7, s67, v5
	v_mov_b32_e32 v147, v195
	v_lshl_add_u64 v[4:5], v[4:5], 0, s[70:71]
	v_mad_i32_i24 v15, v11, s67, v15
	v_lshl_add_u64 v[154:155], v[4:5], 0, v[146:147]
	v_lshl_add_u64 v[4:5], v[14:15], 0, s[70:71]
	v_lshl_add_u64 v[158:159], v[4:5], 0, v[146:147]
	v_cndmask_b32_e64 v4, v16, v17, s[0:1]
	v_add_u32_e32 v4, v4, v163
	v_ashrrev_i32_e32 v9, 31, v8
	v_ashrrev_i32_e32 v5, 31, v4
	v_lshl_add_u64 v[8:9], s[56:57], 0, v[8:9]
	v_lshl_add_u64 v[4:5], s[56:57], 0, v[4:5]
	v_mad_u64_u32 v[12:13], s[58:59], v8, s67, v[2:3]
	v_mad_u64_u32 v[2:3], s[56:57], v4, s67, v[2:3]
	v_mad_i32_i24 v13, v9, s67, v13
	v_mad_i32_i24 v3, v5, s67, v3
	v_lshl_add_u64 v[6:7], v[12:13], 0, s[70:71]
	v_lshl_add_u64 v[2:3], v[2:3], 0, s[70:71]
	v_lshl_add_u64 v[156:157], v[6:7], 0, v[146:147]
	s_mov_b32 s57, s71
	v_lshl_add_u64 v[160:161], v[2:3], 0, v[146:147]
	v_mov_b64_e32 v[6:7], v[110:111]
	v_mov_b64_e32 v[10:11], v[114:115]
	v_mov_b64_e32 v[14:15], v[122:123]
	v_mov_b64_e32 v[18:19], v[126:127]
	v_mov_b64_e32 v[132:133], v[96:97]
	v_mov_b64_e32 v[136:137], v[92:93]
	v_mov_b64_e32 v[140:141], v[88:89]
	v_mov_b64_e32 v[2:3], v[82:83]
	v_mov_b64_e32 v[22:23], v[118:119]
	v_mov_b64_e32 v[26:27], v[106:107]
	v_mov_b64_e32 v[30:31], v[102:103]
	v_mov_b64_e32 v[34:35], v[98:99]
	s_waitcnt vmcnt(0)
	v_mul_f32_e32 v182, 0x3fb8aa3b, v181
	v_writelane_b32 v244, s56, 23
	s_mov_b64 s[58:59], -1
	v_mov_b64_e32 v[8:9], v[112:113]
	v_mov_b64_e32 v[12:13], v[116:117]
	v_mov_b64_e32 v[16:17], v[124:125]
	v_mov_b64_e32 v[20:21], v[128:129]
	v_mov_b64_e32 v[130:131], v[94:95]
	v_mov_b64_e32 v[134:135], v[90:91]
	v_mov_b64_e32 v[138:139], v[86:87]
	v_mov_b64_e32 v[4:5], v[84:85]
	v_mov_b64_e32 v[24:25], v[120:121]
	v_mov_b64_e32 v[28:29], v[108:109]
	v_mov_b64_e32 v[32:33], v[104:105]
	v_mov_b64_e32 v[36:37], v[100:101]
	s_mov_b32 s63, 0
	v_writelane_b32 v244, s57, 24
	s_xor_b64 s[56:57], s[58:59], -1
	s_and_b64 vcc, exec, s[56:57]
	s_mov_b64 s[58:59], -1
	s_cbranch_vccz .LBB0_1884
